# P14 combine/final-norm row loop de-serialised: final-norm gain hoisted out of the loop (registers), slot indices prefetched one row ahead, 8 row stores issued back to back (no load+vmcnt(0) ladder); d
# speedup vs baseline: 1.0072x; 1.0072x over previous
.LBB0_2426:
	s_cmp_gt_i32 s92, 14
	s_cselect_b64 s[0:1], -1, 0
	s_cmp_lt_i32 s93, 15
	s_cselect_b64 s[2:3], -1, 0
	s_or_b64 s[0:1], s[0:1], s[2:3]
	s_and_b64 vcc, exec, s[0:1]
	v_mbcnt_lo_u32_b32 v40, -1, 0
	v_mbcnt_hi_u32_b32 v40, -1, v40
	s_cbranch_vccnz .LBB0_2430
	s_lshl_b32 s0, s94, 3
	s_add_i32 s2, s97, s0
	s_cmpk_gt_i32 s2, 0x7fff
	s_cbranch_scc1 .LBB0_2430
	s_load_dwordx2 s[0:1], s[90:91], 0xd8
	v_ashrrev_i32_e32 v41, 31, v40
	s_waitcnt lgkmcnt(0)
	v_lshl_add_u64 v[0:1], v[40:41], 2, s[26:27]
	s_mov_b64 s[4:5], 0x5e000000
	v_lshl_add_u64 v[42:43], v[0:1], 0, s[4:5]
	v_lshlrev_b64 v[0:1], 4, v[40:41]
	v_lshl_add_u64 v[44:45], s[0:1], 0, v[0:1]
	s_mov_b64 s[4:5], 0x1400
	v_lshl_add_u64 v[48:49], v[44:45], 0, s[4:5]
	s_mov_b64 s[4:5], 0x1800
	v_lshl_add_u64 v[50:51], v[44:45], 0, s[4:5]
	s_mov_b64 s[4:5], 0x1c00
	v_readlane_b32 s3, v254, 0
	v_lshl_add_u64 v[52:53], v[44:45], 0, s[4:5]
	s_lshl_b32 s4, s3, 3
	s_ashr_i32 s3, s2, 31
	s_lshl_b64 s[6:7], s[2:3], 13
	s_add_u32 s6, s24, s6
	s_addc_u32 s7, s25, s7
	s_mov_b64 s[0:1], 0x1000
	v_lshl_add_u64 v[0:1], s[6:7], 0, v[0:1]
	s_ashr_i32 s5, s4, 31
	v_lshl_add_u64 v[46:47], v[44:45], 0, s[0:1]
	v_lshl_add_u64 v[54:55], v[0:1], 0, s[0:1]
	s_lshl_b64 s[6:7], s[4:5], 13
	s_lshl_b64 s[0:1], s[2:3], 4
	s_add_u32 s0, s26, s0
	s_addc_u32 s1, s27, s1
	s_add_u32 s8, s0, 0xe00008
	s_addc_u32 s9, s1, 0
	s_lshl_b64 s[10:11], s[4:5], 4
	v_mov_b32_e32 v56, 0
	s_mov_b64 s[12:13], 0x80a000
	s_mov_b32 s14, 0x3d800000
	s_mov_b32 s3, 0x80b000
	v_mov_b32_e32 v57, 0x358637bd
	s_mov_b32 s5, 0xf800000
	v_mov_b32_e32 v58, 0x260
	global_load_dwordx4 v[248:251], v56, s[8:9] offset:-8
	global_load_dwordx4 v[216:219], v[44:45], off
	global_load_dwordx4 v[220:223], v[44:45], off offset:1024
	global_load_dwordx4 v[224:227], v[44:45], off offset:2048
	global_load_dwordx4 v[228:231], v[44:45], off offset:3072
	global_load_dwordx4 v[232:235], v[46:47], off
	global_load_dwordx4 v[236:239], v[48:49], off
	global_load_dwordx4 v[240:243], v[50:51], off
	global_load_dwordx4 v[244:247], v[52:53], off
	s_add_u32 s8, s8, s10
	s_addc_u32 s9, s9, s11
.LBB0_2429:
	s_ashr_i32 s0, s2, 11
	s_mul_hi_i32 s1, s0, 0xc000
	s_mul_i32 s0, s0, 0xc000
	s_add_u32 s0, s26, s0
	s_addc_u32 s1, s27, s1
	v_lshl_add_u64 v[60:61], v[40:41], 4, s[0:1]
	v_add_co_u32_e32 v90, vcc, s3, v60
	v_lshl_add_u64 v[88:89], v[60:61], 0, s[12:13]
	s_nop 0
	v_addc_co_u32_e32 v91, vcc, 0, v61, vcc
	global_load_dwordx4 v[0:3], v[54:55], off offset:-4096 nt
	global_load_dwordx4 v[4:7], v[54:55], off offset:-3072 nt
	global_load_dwordx4 v[8:11], v[54:55], off offset:-2048 nt
	global_load_dwordx4 v[12:15], v[54:55], off offset:-1024 nt
	global_load_dwordx4 v[20:23], v[54:55], off nt
	global_load_dwordx4 v[24:27], v[54:55], off offset:1024 nt
	global_load_dwordx4 v[28:31], v[54:55], off offset:2048 nt
	global_load_dwordx4 v[36:39], v[54:55], off offset:3072 nt
	global_load_dwordx4 v[60:63], v[88:89], off offset:1024
	global_load_dwordx4 v[64:67], v[88:89], off offset:2048
	global_load_dwordx4 v[16:19], v[88:89], off offset:3072
	global_load_dwordx4 v[68:71], v[90:91], off offset:-4096
	global_load_dwordx4 v[72:75], v[90:91], off
	global_load_dwordx4 v[76:79], v[90:91], off offset:1024
	global_load_dwordx4 v[80:83], v[90:91], off offset:2048
	global_load_dwordx4 v[84:87], v[90:91], off offset:3072
	s_waitcnt vmcnt(24)
	v_ashrrev_i32_e32 v91, 31, v248
	v_mov_b32_e32 v90, v248
	v_ashrrev_i32_e32 v93, 31, v249
	v_mov_b32_e32 v92, v249
	v_ashrrev_i32_e32 v33, 31, v250
	v_mov_b32_e32 v32, v250
	v_ashrrev_i32_e32 v95, 31, v251
	v_mov_b32_e32 v94, v251
	v_lshlrev_b64 v[34:35], 11, v[92:93]
	v_lshlrev_b64 v[90:91], 11, v[90:91]
	v_lshlrev_b64 v[92:93], 11, v[94:95]
	v_lshlrev_b64 v[32:33], 11, v[32:33]
	v_lshl_add_u64 v[90:91], v[42:43], 0, v[90:91]
	v_lshl_add_u64 v[34:35], v[42:43], 0, v[34:35]
	v_lshl_add_u64 v[94:95], v[42:43], 0, v[32:33]
	v_lshl_add_u64 v[92:93], v[42:43], 0, v[92:93]
	global_load_dword v59, v[90:91], off nt
	global_load_dword v96, v[34:35], off nt
	global_load_dword v98, v[94:95], off nt
	global_load_dword v102, v[92:93], off nt
	global_load_dword v106, v[90:91], off offset:256 nt
	global_load_dword v110, v[34:35], off offset:256 nt
	global_load_dword v114, v[94:95], off offset:256 nt
	global_load_dword v118, v[92:93], off offset:256 nt
	global_load_dword v122, v[90:91], off offset:512 nt
	global_load_dword v126, v[34:35], off offset:512 nt
	global_load_dword v130, v[94:95], off offset:512 nt
	global_load_dword v134, v[92:93], off offset:512 nt
	global_load_dword v138, v[90:91], off offset:768 nt
	global_load_dword v142, v[34:35], off offset:768 nt
	global_load_dword v146, v[94:95], off offset:768 nt
	global_load_dword v150, v[92:93], off offset:768 nt
	global_load_dword v154, v[90:91], off offset:1024 nt
	global_load_dword v158, v[34:35], off offset:1024 nt
	global_load_dword v162, v[94:95], off offset:1024 nt
	global_load_dword v166, v[92:93], off offset:1024 nt
	global_load_dword v170, v[90:91], off offset:1280 nt
	global_load_dword v174, v[34:35], off offset:1280 nt
	global_load_dword v178, v[94:95], off offset:1280 nt
	global_load_dword v182, v[92:93], off offset:1280 nt
	global_load_dword v186, v[90:91], off offset:1536 nt
	global_load_dword v190, v[34:35], off offset:1536 nt
	global_load_dword v194, v[94:95], off offset:1536 nt
	global_load_dword v198, v[92:93], off offset:1536 nt
	global_load_dword v202, v[90:91], off offset:1792 nt
	global_load_dword v206, v[34:35], off offset:1792 nt
	global_load_dword v210, v[94:95], off offset:1792 nt
	global_load_dword v214, v[92:93], off offset:1792 nt
	global_load_dwordx4 v[248:251], v56, s[8:9] offset:-8
	s_add_u32 s8, s8, s10
	s_addc_u32 s9, s9, s11
	s_add_i32 s2, s2, s4
	s_cmp_lt_i32 s2, 0x8000
	s_waitcnt vmcnt(32)
	v_cvt_pk_f32_fp8_e32 v[88:89], v59
	v_cvt_pk_f32_fp8_sdwa v[90:91], v59 src0_sel:WORD_1
	s_waitcnt vmcnt(31)
	v_cvt_pk_f32_fp8_e32 v[92:93], v96
	v_cvt_pk_f32_fp8_sdwa v[94:95], v96 src0_sel:WORD_1
	s_waitcnt vmcnt(30)
	v_cvt_pk_f32_fp8_e32 v[96:97], v98
	v_cvt_pk_f32_fp8_sdwa v[98:99], v98 src0_sel:WORD_1
	s_waitcnt vmcnt(29)
	v_cvt_pk_f32_fp8_e32 v[100:101], v102
	v_cvt_pk_f32_fp8_sdwa v[102:103], v102 src0_sel:WORD_1
	s_waitcnt vmcnt(28)
	v_cvt_pk_f32_fp8_e32 v[104:105], v106
	v_cvt_pk_f32_fp8_sdwa v[106:107], v106 src0_sel:WORD_1
	s_waitcnt vmcnt(27)
	v_cvt_pk_f32_fp8_e32 v[108:109], v110
	v_cvt_pk_f32_fp8_sdwa v[110:111], v110 src0_sel:WORD_1
	s_waitcnt vmcnt(26)
	v_cvt_pk_f32_fp8_e32 v[112:113], v114
	v_cvt_pk_f32_fp8_sdwa v[114:115], v114 src0_sel:WORD_1
	s_waitcnt vmcnt(25)
	v_cvt_pk_f32_fp8_e32 v[116:117], v118
	v_cvt_pk_f32_fp8_sdwa v[118:119], v118 src0_sel:WORD_1
	s_waitcnt vmcnt(24)
	v_cvt_pk_f32_fp8_e32 v[120:121], v122
	v_cvt_pk_f32_fp8_sdwa v[122:123], v122 src0_sel:WORD_1
	s_waitcnt vmcnt(23)
	v_cvt_pk_f32_fp8_e32 v[124:125], v126
	v_cvt_pk_f32_fp8_sdwa v[126:127], v126 src0_sel:WORD_1
	s_waitcnt vmcnt(22)
	v_cvt_pk_f32_fp8_e32 v[128:129], v130
	v_cvt_pk_f32_fp8_sdwa v[130:131], v130 src0_sel:WORD_1
	s_waitcnt vmcnt(21)
	v_cvt_pk_f32_fp8_e32 v[132:133], v134
	v_cvt_pk_f32_fp8_sdwa v[134:135], v134 src0_sel:WORD_1
	s_waitcnt vmcnt(20)
	v_cvt_pk_f32_fp8_e32 v[136:137], v138
	v_cvt_pk_f32_fp8_sdwa v[138:139], v138 src0_sel:WORD_1
	s_waitcnt vmcnt(19)
	v_cvt_pk_f32_fp8_e32 v[140:141], v142
	v_cvt_pk_f32_fp8_sdwa v[142:143], v142 src0_sel:WORD_1
	s_waitcnt vmcnt(18)
	v_cvt_pk_f32_fp8_e32 v[144:145], v146
	v_cvt_pk_f32_fp8_sdwa v[146:147], v146 src0_sel:WORD_1
	s_waitcnt vmcnt(17)
	v_cvt_pk_f32_fp8_e32 v[148:149], v150
	v_cvt_pk_f32_fp8_sdwa v[150:151], v150 src0_sel:WORD_1
	s_waitcnt vmcnt(16)
	v_cvt_pk_f32_fp8_e32 v[152:153], v154
	s_waitcnt vmcnt(15)
	v_cvt_pk_f32_fp8_e32 v[156:157], v158
	s_waitcnt vmcnt(14)
	v_cvt_pk_f32_fp8_e32 v[160:161], v162
	s_waitcnt vmcnt(13)
	v_cvt_pk_f32_fp8_e32 v[164:165], v166
	s_waitcnt vmcnt(12)
	v_cvt_pk_f32_fp8_e32 v[168:169], v170
	v_cvt_pk_f32_fp8_sdwa v[170:171], v170 src0_sel:WORD_1
	s_waitcnt vmcnt(11)
	v_cvt_pk_f32_fp8_e32 v[172:173], v174
	v_cvt_pk_f32_fp8_sdwa v[174:175], v174 src0_sel:WORD_1
	s_waitcnt vmcnt(10)
	v_cvt_pk_f32_fp8_e32 v[176:177], v178
	v_cvt_pk_f32_fp8_sdwa v[178:179], v178 src0_sel:WORD_1
	s_waitcnt vmcnt(9)
	v_cvt_pk_f32_fp8_e32 v[180:181], v182
	v_cvt_pk_f32_fp8_sdwa v[182:183], v182 src0_sel:WORD_1
	s_waitcnt vmcnt(8)
	v_cvt_pk_f32_fp8_e32 v[184:185], v186
	s_waitcnt vmcnt(7)
	v_cvt_pk_f32_fp8_e32 v[188:189], v190
	s_waitcnt vmcnt(6)
	v_cvt_pk_f32_fp8_e32 v[192:193], v194
	s_waitcnt vmcnt(5)
	v_cvt_pk_f32_fp8_e32 v[196:197], v198
	s_waitcnt vmcnt(4)
	v_cvt_pk_f32_fp8_e32 v[200:201], v202
	v_cvt_pk_f32_fp8_sdwa v[202:203], v202 src0_sel:WORD_1
	s_waitcnt vmcnt(3)
	v_cvt_pk_f32_fp8_e32 v[204:205], v206
	v_cvt_pk_f32_fp8_sdwa v[206:207], v206 src0_sel:WORD_1
	s_waitcnt vmcnt(2)
	v_cvt_pk_f32_fp8_e32 v[208:209], v210
	v_cvt_pk_f32_fp8_sdwa v[210:211], v210 src0_sel:WORD_1
	s_waitcnt vmcnt(1)
	v_cvt_pk_f32_fp8_e32 v[212:213], v214
	v_cvt_pk_f32_fp8_sdwa v[214:215], v214 src0_sel:WORD_1
	v_cvt_pk_f32_fp8_sdwa v[154:155], v154 src0_sel:WORD_1
	v_cvt_pk_f32_fp8_sdwa v[158:159], v158 src0_sel:WORD_1
	v_cvt_pk_f32_fp8_sdwa v[162:163], v162 src0_sel:WORD_1
	v_cvt_pk_f32_fp8_sdwa v[166:167], v166 src0_sel:WORD_1
	v_cvt_pk_f32_fp8_sdwa v[186:187], v186 src0_sel:WORD_1
	v_cvt_pk_f32_fp8_sdwa v[190:191], v190 src0_sel:WORD_1
	v_cvt_pk_f32_fp8_sdwa v[194:195], v194 src0_sel:WORD_1
	v_cvt_pk_f32_fp8_sdwa v[198:199], v198 src0_sel:WORD_1
	v_pk_add_f32 v[88:89], v[88:89], v[92:93]
	v_pk_add_f32 v[90:91], v[90:91], v[94:95]
	v_pk_add_f32 v[92:93], v[96:97], v[100:101]
	v_pk_add_f32 v[94:95], v[98:99], v[102:103]
	v_pk_add_f32 v[96:97], v[104:105], v[108:109]
	v_pk_add_f32 v[98:99], v[106:107], v[110:111]
	v_pk_add_f32 v[100:101], v[112:113], v[116:117]
	v_pk_add_f32 v[102:103], v[114:115], v[118:119]
	v_pk_add_f32 v[104:105], v[120:121], v[124:125]
	v_pk_add_f32 v[106:107], v[122:123], v[126:127]
	v_pk_add_f32 v[108:109], v[128:129], v[132:133]
	v_pk_add_f32 v[110:111], v[130:131], v[134:135]
	v_pk_add_f32 v[112:113], v[136:137], v[140:141]
	v_pk_add_f32 v[114:115], v[138:139], v[142:143]
	v_pk_add_f32 v[116:117], v[144:145], v[148:149]
	v_pk_add_f32 v[118:119], v[146:147], v[150:151]
	v_pk_add_f32 v[120:121], v[152:153], v[156:157]
	v_pk_add_f32 v[124:125], v[160:161], v[164:165]
	v_pk_add_f32 v[130:131], v[170:171], v[174:175]
	v_pk_add_f32 v[134:135], v[178:179], v[182:183]
	v_pk_add_f32 v[136:137], v[184:185], v[188:189]
	v_pk_add_f32 v[140:141], v[192:193], v[196:197]
	v_pk_add_f32 v[146:147], v[202:203], v[206:207]
	v_pk_add_f32 v[150:151], v[210:211], v[214:215]
	v_pk_add_f32 v[88:89], v[88:89], v[92:93]
	v_pk_add_f32 v[90:91], v[90:91], v[94:95]
	v_pk_add_f32 v[92:93], v[96:97], v[100:101]
	v_pk_add_f32 v[94:95], v[98:99], v[102:103]
	v_pk_add_f32 v[122:123], v[154:155], v[158:159]
	v_pk_add_f32 v[126:127], v[162:163], v[166:167]
	v_pk_add_f32 v[128:129], v[168:169], v[172:173]
	v_pk_add_f32 v[132:133], v[176:177], v[180:181]
	v_pk_add_f32 v[138:139], v[186:187], v[190:191]
	v_pk_add_f32 v[142:143], v[194:195], v[198:199]
	v_pk_add_f32 v[144:145], v[200:201], v[204:205]
	v_pk_add_f32 v[148:149], v[208:209], v[212:213]
	v_pk_add_f32 v[96:97], v[104:105], v[108:109]
	v_pk_add_f32 v[98:99], v[106:107], v[110:111]
	v_pk_add_f32 v[100:101], v[112:113], v[116:117]
	v_pk_add_f32 v[102:103], v[114:115], v[118:119]
	v_pk_add_f32 v[104:105], v[120:121], v[124:125]
	v_pk_add_f32 v[110:111], v[130:131], v[134:135]
	v_pk_add_f32 v[112:113], v[136:137], v[140:141]
	v_pk_add_f32 v[118:119], v[146:147], v[150:151]
	v_pk_mul_f32 v[88:89], v[88:89], s[14:15] op_sel_hi:[1,0]
	v_pk_mul_f32 v[90:91], v[90:91], s[14:15] op_sel_hi:[1,0]
	v_pk_mul_f32 v[92:93], v[92:93], s[14:15] op_sel_hi:[1,0]
	v_pk_mul_f32 v[94:95], v[94:95], s[14:15] op_sel_hi:[1,0]
	v_pk_add_f32 v[106:107], v[122:123], v[126:127]
	v_pk_add_f32 v[108:109], v[128:129], v[132:133]
	v_pk_add_f32 v[114:115], v[138:139], v[142:143]
	v_pk_add_f32 v[116:117], v[144:145], v[148:149]
	v_pk_mul_f32 v[98:99], v[98:99], s[14:15] op_sel_hi:[1,0]
	v_pk_mul_f32 v[96:97], v[96:97], s[14:15] op_sel_hi:[1,0]
	v_pk_mul_f32 v[102:103], v[102:103], s[14:15] op_sel_hi:[1,0]
	v_pk_mul_f32 v[104:105], v[104:105], s[14:15] op_sel_hi:[1,0]
	v_pk_mul_f32 v[110:111], v[110:111], s[14:15] op_sel_hi:[1,0]
	v_pk_mul_f32 v[112:113], v[112:113], s[14:15] op_sel_hi:[1,0]
	v_pk_mul_f32 v[118:119], v[118:119], s[14:15] op_sel_hi:[1,0]
	v_pk_fma_f32 v[2:3], v[70:71], v[90:91], v[2:3]
	v_pk_fma_f32 v[0:1], v[68:69], v[88:89], v[0:1]
	v_pk_fma_f32 v[6:7], v[62:63], v[94:95], v[6:7]
	v_pk_fma_f32 v[4:5], v[60:61], v[92:93], v[4:5]
	v_pk_mul_f32 v[100:101], v[100:101], s[14:15] op_sel_hi:[1,0]
	v_pk_mul_f32 v[106:107], v[106:107], s[14:15] op_sel_hi:[1,0]
	v_pk_mul_f32 v[108:109], v[108:109], s[14:15] op_sel_hi:[1,0]
	v_pk_mul_f32 v[114:115], v[114:115], s[14:15] op_sel_hi:[1,0]
	v_pk_mul_f32 v[116:117], v[116:117], s[14:15] op_sel_hi:[1,0]
	v_pk_fma_f32 v[8:9], v[64:65], v[96:97], v[8:9]
	v_pk_fma_f32 v[10:11], v[66:67], v[98:99], v[10:11]
	s_waitcnt vmcnt(1)
	v_pk_fma_f32 v[14:15], v[18:19], v[102:103], v[14:15]
	v_pk_fma_f32 v[18:19], v[72:73], v[104:105], v[20:21]
	v_pk_fma_f32 v[20:21], v[78:79], v[110:111], v[26:27]
	v_pk_fma_f32 v[26:27], v[80:81], v[112:113], v[28:29]
	v_pk_fma_f32 v[28:29], v[86:87], v[118:119], v[38:39]
	v_mov_b32_e32 v38, v1
	v_mov_b32_e32 v39, v5
	v_mov_b32_e32 v62, v3
	v_mov_b32_e32 v63, v7
	v_pk_fma_f32 v[12:13], v[16:17], v[100:101], v[12:13]
	v_pk_fma_f32 v[16:17], v[74:75], v[106:107], v[22:23]
	v_pk_fma_f32 v[22:23], v[76:77], v[108:109], v[24:25]
	v_pk_fma_f32 v[24:25], v[82:83], v[114:115], v[30:31]
	v_pk_fma_f32 v[30:31], v[84:85], v[116:117], v[36:37]
	v_mov_b32_e32 v36, v0
	v_mov_b32_e32 v37, v4
	v_mov_b32_e32 v60, v2
	v_mov_b32_e32 v61, v6
	v_pk_mul_f32 v[64:65], v[10:11], v[10:11]
	v_pk_mul_f32 v[66:67], v[8:9], v[8:9]
	v_pk_mul_f32 v[38:39], v[38:39], v[38:39]
	v_pk_mul_f32 v[62:63], v[62:63], v[62:63]
	v_pk_mov_b32 v[80:81], v[66:67], v[64:65] op_sel:[1,0]
	v_mov_b32_e32 v67, v65
	v_pk_fma_f32 v[36:37], v[36:37], v[36:37], v[38:39]
	v_pk_fma_f32 v[38:39], v[60:61], v[60:61], v[62:63]
	v_mul_f32_e32 v68, v13, v13
	v_mul_f32_e32 v70, v15, v15
	v_pk_add_f32 v[60:61], v[80:81], v[66:67]
	v_pk_add_f32 v[36:37], v[36:37], v[38:39]
	v_mul_f32_e32 v59, v18, v18
	v_mul_f32_e32 v79, v19, v19
	v_mul_f32_e32 v82, v16, v16
	v_mul_f32_e32 v83, v17, v17
	v_pk_fma_f32 v[64:65], v[12:13], v[12:13], v[68:69] op_sel_hi:[1,1,0]
	v_pk_fma_f32 v[68:69], v[14:15], v[14:15], v[70:71] op_sel_hi:[1,1,0]
	v_pk_add_f32 v[38:39], v[60:61], v[60:61] op_sel:[0,1] op_sel_hi:[1,0]
	v_pk_add_f32 v[36:37], v[36:37], v[36:37] op_sel:[0,1] op_sel_hi:[1,0]
	v_pk_mul_f32 v[72:73], v[20:21], v[20:21]
	v_pk_mul_f32 v[74:75], v[22:23], v[22:23]
	v_mov_b32_e32 v65, v82
	v_mov_b32_e32 v69, v83
	v_mov_b32_e32 v39, v79
	v_mov_b32_e32 v37, v59
	v_pk_mov_b32 v[70:71], v[74:75], v[72:73] op_sel:[1,0]
	v_mov_b32_e32 v75, v73
	v_pk_add_f32 v[60:61], v[64:65], v[68:69]
	v_pk_add_f32 v[36:37], v[36:37], v[38:39]
	v_mul_f32_e32 v76, v27, v27
	v_mul_f32_e32 v78, v25, v25
	v_pk_add_f32 v[62:63], v[70:71], v[74:75]
	v_pk_add_f32 v[36:37], v[36:37], v[60:61]
	v_mul_f32_e32 v84, v30, v30
	v_mul_f32_e32 v85, v31, v31
	v_mul_f32_e32 v86, v28, v28
	v_mul_f32_e32 v87, v29, v29
	v_pk_fma_f32 v[72:73], v[26:27], v[26:27], v[76:77] op_sel_hi:[1,1,0]
	v_pk_fma_f32 v[76:77], v[24:25], v[24:25], v[78:79] op_sel_hi:[1,1,0]
	v_pk_add_f32 v[62:63], v[62:63], v[62:63] op_sel:[0,1] op_sel_hi:[1,0]
	v_pk_add_f32 v[36:37], v[36:37], v[36:37] op_sel:[0,1] op_sel_hi:[1,0]
	v_mov_b32_e32 v73, v86
	v_mov_b32_e32 v77, v87
	v_mov_b32_e32 v63, v85
	v_mov_b32_e32 v37, v84
	v_pk_add_f32 v[64:65], v[72:73], v[76:77]
	v_pk_add_f32 v[36:37], v[36:37], v[62:63]
	s_nop 0
	v_pk_add_f32 v[36:37], v[36:37], v[64:65]
	s_nop 0
	v_add_f32_e32 v36, v36, v37
	s_nop 1
	v_add_f32_dpp v36, v36, v36 quad_perm:[1,0,3,2] row_mask:0xf bank_mask:0xf bound_ctrl:1
	s_nop 1
	v_add_f32_dpp v36, v36, v36 quad_perm:[2,3,0,1] row_mask:0xf bank_mask:0xf bound_ctrl:1
	s_nop 1
	v_add_f32_dpp v36, v36, v36 row_ror:4 row_mask:0xf bank_mask:0xf bound_ctrl:1
	s_nop 1
	v_add_f32_dpp v36, v36, v36 row_ror:8 row_mask:0xf bank_mask:0xf bound_ctrl:1
	s_nop 0
	v_readlane_b32 s15, v36, 16
	v_readlane_b32 s16, v36, 48
	v_readlane_b32 s0, v36, 0
	v_readlane_b32 s1, v36, 32
	v_mov_b32_e32 v36, s15
	v_mov_b32_e32 v37, s16
	v_pk_add_f32 v[36:37], s[0:1], v[36:37]
	s_nop 0
	v_add_f32_e32 v36, v36, v37
	v_fmamk_f32 v36, v36, 0x3a000000, v57
	v_mul_f32_e32 v37, 0x4f800000, v36
	v_cmp_gt_f32_e32 vcc, s5, v36
	s_nop 1
	v_cndmask_b32_e32 v36, v36, v37, vcc
	v_sqrt_f32_e32 v37, v36
	s_nop 0
	v_add_u32_e32 v38, -1, v37
	v_add_u32_e32 v39, 1, v37
	v_fma_f32 v59, -v38, v37, v36
	v_fma_f32 v60, -v39, v37, v36
	v_cmp_ge_f32_e64 s[0:1], 0, v59
	s_nop 1
	v_cndmask_b32_e64 v37, v37, v38, s[0:1]
	v_cmp_lt_f32_e64 s[0:1], 0, v60
	s_nop 1
	v_cndmask_b32_e64 v37, v37, v39, s[0:1]
	v_mul_f32_e32 v38, 0x37800000, v37
	v_cndmask_b32_e32 v37, v37, v38, vcc
	v_cmp_class_f32_e32 vcc, v36, v58
	s_nop 1
	v_cndmask_b32_e32 v36, v37, v36, vcc
	v_div_scale_f32 v37, s[0:1], v36, v36, 1.0
	v_rcp_f32_e32 v39, v37
	v_div_scale_f32 v38, vcc, 1.0, v36, 1.0
	v_fma_f32 v59, -v37, v39, 1.0
	v_fmac_f32_e32 v39, v59, v39
	v_mul_f32_e32 v59, v38, v39
	v_fma_f32 v60, -v37, v59, v38
	v_fmac_f32_e32 v59, v60, v39
	v_fma_f32 v37, -v37, v59, v38
	v_div_fmas_f32 v37, v37, v39, v59
	v_div_fixup_f32 v36, v37, v36, 1.0
	v_pk_mul_f32 v[0:1], v[0:1], v[36:37] op_sel_hi:[1,0]
	v_pk_mul_f32 v[2:3], v[2:3], v[36:37] op_sel_hi:[1,0]
	v_pk_mul_f32 v[0:1], v[216:217], v[0:1]
	v_pk_mul_f32 v[2:3], v[218:219], v[2:3]
	global_store_dwordx4 v[54:55], v[0:3], off offset:-4096 nt
	v_pk_mul_f32 v[4:5], v[4:5], v[36:37] op_sel_hi:[1,0]
	v_pk_mul_f32 v[6:7], v[6:7], v[36:37] op_sel_hi:[1,0]
	v_pk_mul_f32 v[4:5], v[220:221], v[4:5]
	v_pk_mul_f32 v[6:7], v[222:223], v[6:7]
	global_store_dwordx4 v[54:55], v[4:7], off offset:-3072 nt
	v_pk_mul_f32 v[8:9], v[8:9], v[36:37] op_sel_hi:[1,0]
	v_pk_mul_f32 v[10:11], v[10:11], v[36:37] op_sel_hi:[1,0]
	v_pk_mul_f32 v[8:9], v[224:225], v[8:9]
	v_pk_mul_f32 v[10:11], v[226:227], v[10:11]
	global_store_dwordx4 v[54:55], v[8:11], off offset:-2048 nt
	v_pk_mul_f32 v[12:13], v[12:13], v[36:37] op_sel_hi:[1,0]
	v_pk_mul_f32 v[14:15], v[14:15], v[36:37] op_sel_hi:[1,0]
	v_pk_mul_f32 v[12:13], v[228:229], v[12:13]
	v_pk_mul_f32 v[14:15], v[230:231], v[14:15]
	global_store_dwordx4 v[54:55], v[12:15], off offset:-1024 nt
	v_pk_mul_f32 v[18:19], v[18:19], v[36:37] op_sel_hi:[1,0]
	v_pk_mul_f32 v[16:17], v[16:17], v[36:37] op_sel_hi:[1,0]
	v_pk_mul_f32 v[32:33], v[232:233], v[18:19]
	v_pk_mul_f32 v[34:35], v[234:235], v[16:17]
	global_store_dwordx4 v[54:55], v[32:35], off nt
	v_pk_mul_f32 v[22:23], v[22:23], v[36:37] op_sel_hi:[1,0]
	v_pk_mul_f32 v[20:21], v[20:21], v[36:37] op_sel_hi:[1,0]
	v_pk_mul_f32 v[60:61], v[236:237], v[22:23]
	v_pk_mul_f32 v[62:63], v[238:239], v[20:21]
	global_store_dwordx4 v[54:55], v[60:63], off offset:1024 nt
	v_pk_mul_f32 v[26:27], v[26:27], v[36:37] op_sel_hi:[1,0]
	v_pk_mul_f32 v[24:25], v[24:25], v[36:37] op_sel_hi:[1,0]
	v_pk_mul_f32 v[64:65], v[240:241], v[26:27]
	v_pk_mul_f32 v[66:67], v[242:243], v[24:25]
	global_store_dwordx4 v[54:55], v[64:67], off offset:2048 nt
	v_pk_mul_f32 v[30:31], v[30:31], v[36:37] op_sel_hi:[1,0]
	v_pk_mul_f32 v[28:29], v[28:29], v[36:37] op_sel_hi:[1,0]
	v_pk_mul_f32 v[68:69], v[244:245], v[30:31]
	v_pk_mul_f32 v[70:71], v[246:247], v[28:29]
	global_store_dwordx4 v[54:55], v[68:71], off offset:3072 nt
	v_lshl_add_u64 v[54:55], v[54:55], 0, s[6:7]
	s_cbranch_scc1 .LBB0_2429
